# v48 + waves 4-7 delayed half a tile iteration in the indexer loop (stagger MFMA vs VALU of the two waves per SIMD)
# speedup vs baseline: 1.0044x; 1.0043x over previous
.LBB0_404:
	s_lshl_b32 s12, s12, 10
	s_lshl_b32 s0, s13, 6
	s_add_i32 s1, s12, 0x400
	s_add_i32 s13, s0, 64
	s_min_u32 s1, s1, s13
	s_sub_i32 s1, s1, s12
	s_ashr_i32 s24, s1, 5
	s_cmp_lt_i32 s24, 1
	s_cbranch_scc1 .LBB0_407
	s_mul_i32 s13, s4, 0x3400000
	s_mul_hi_u32 s1, s4, 0x3400000
	s_add_u32 s14, s82, s13
	s_addc_u32 s15, s83, s1
	s_add_i32 s13, s0, s17
	v_or_b32_e32 v4, s13, v158
	v_mov_b64_e32 v[2:3], s[14:15]
	v_mad_u64_u32 v[4:5], s[0:1], v4, s18, v[2:3]
	s_or_b32 s25, s13, 2
	v_lshl_add_u64 v[4:5], v[4:5], 0, v[144:145]
	s_waitcnt vmcnt(30)
	v_or_b32_e32 v6, s25, v158
	v_lshl_add_u64 v[4:5], v[4:5], 0, v[148:149]
	v_mad_u64_u32 v[6:7], s[0:1], v6, s18, v[2:3]
	s_waitcnt vmcnt(22)
	v_lshl_add_u64 v[38:39], v[4:5], 0, s[6:7]
	v_add_co_u32_e32 v4, vcc, s19, v4
	v_lshl_add_u64 v[6:7], v[6:7], 0, v[144:145]
	s_nop 0
	v_addc_co_u32_e32 v5, vcc, 0, v5, vcc
	v_lshl_add_u64 v[6:7], v[6:7], 0, v[148:149]
	s_or_b32 s26, s13, 4
	global_load_dwordx4 v[66:69], v[38:39], off offset:64
	global_load_dwordx4 v[70:73], v[38:39], off offset:96
	v_lshl_add_u64 v[8:9], v[6:7], 0, s[6:7]
	global_load_dwordx4 v[74:77], v[4:5], off offset:2560
	global_load_dwordx4 v[78:81], v[8:9], off offset:32
	global_load_dwordx4 v[82:85], v[8:9], off offset:64
	global_load_dwordx4 v[86:89], v[8:9], off offset:96
	v_or_b32_e32 v4, s26, v158
	v_mad_u64_u32 v[4:5], s[0:1], v4, s18, v[2:3]
	v_add_co_u32_e32 v18, vcc, s19, v6
	v_lshl_add_u64 v[4:5], v[4:5], 0, v[144:145]
	s_nop 0
	v_addc_co_u32_e32 v19, vcc, 0, v7, vcc
	v_lshl_add_u64 v[4:5], v[4:5], 0, v[148:149]
	v_add_u32_e32 v6, s25, v142
	v_lshl_add_u64 v[20:21], v[4:5], 0, s[6:7]
	v_add_co_u32_e32 v4, vcc, s19, v4
	v_mad_i64_i32 v[22:23], s[0:1], v6, s18, v[2:3]
	v_add_u32_e32 v6, s13, v142
	v_addc_co_u32_e32 v5, vcc, 0, v5, vcc
	v_mad_i64_i32 v[10:11], s[0:1], v6, s18, v[2:3]
	v_add_co_u32_e32 v6, vcc, s20, v10
	s_or_b32 s25, s13, 6
	s_nop 0
	v_addc_co_u32_e32 v7, vcc, 0, v11, vcc
	v_or_b32_e32 v28, s25, v158
	v_add_co_u32_e32 v12, vcc, s20, v22
	v_mad_u64_u32 v[28:29], s[0:1], v28, s18, v[2:3]
	s_nop 0
	v_addc_co_u32_e32 v13, vcc, 0, v23, vcc
	v_lshl_add_u64 v[14:15], v[10:11], 0, s[10:11]
	v_lshl_add_u64 v[28:29], v[28:29], 0, v[144:145]
	global_load_dwordx4 v[6:9], v[6:7], off offset:640
	s_nop 0
	global_load_dwordx4 v[10:13], v[12:13], off offset:640
	s_nop 0
	global_load_dwordx4 v[14:17], v[14:15], off offset:16
	s_nop 0
	global_load_dwordx4 v[90:93], v[18:19], off offset:2560
	global_load_dwordx4 v[94:97], v[20:21], off offset:32
	global_load_dwordx4 v[98:101], v[20:21], off offset:64
	global_load_dwordx4 v[102:105], v[20:21], off offset:96
	v_add_u32_e32 v18, s26, v142
	v_lshl_add_u64 v[34:35], v[28:29], 0, v[148:149]
	v_add_u32_e32 v28, s25, v142
	v_mad_i64_i32 v[26:27], s[0:1], v18, s18, v[2:3]
	v_mad_i64_i32 v[2:3], s[0:1], v28, s18, v[2:3]
	v_add_co_u32_e32 v18, vcc, s20, v26
	v_add_co_u32_e64 v28, s[0:1], s20, v2
	s_nop 0
	v_addc_co_u32_e32 v19, vcc, 0, v27, vcc
	v_lshl_add_u64 v[22:23], v[22:23], 0, s[10:11]
	v_addc_co_u32_e64 v29, s[0:1], 0, v3, s[0:1]
	v_lshl_add_u64 v[30:31], v[26:27], 0, s[10:11]
	global_load_dwordx4 v[18:21], v[18:19], off offset:640
	s_nop 0
	global_load_dwordx4 v[22:25], v[22:23], off offset:16
	v_lshl_add_u64 v[36:37], v[34:35], 0, s[6:7]
	global_load_dwordx4 v[26:29], v[28:29], off offset:640
	s_nop 0
	global_load_dwordx4 v[30:33], v[30:31], off offset:16
	s_nop 0
	global_load_dwordx4 v[106:109], v[4:5], off offset:2560
	global_load_dwordx4 v[110:113], v[36:37], off offset:32
	global_load_dwordx4 v[114:117], v[36:37], off offset:64
	global_load_dwordx4 v[118:121], v[36:37], off offset:96
	v_or_b32_e32 v4, s12, v146
	v_mul_u32_u24_e32 v4, 0x1a00, v4
	v_mov_b32_e32 v5, v145
	v_add_co_u32_e32 v34, vcc, s19, v34
	v_lshl_add_u64 v[4:5], v[4:5], 1, s[14:15]
	s_nop 0
	v_addc_co_u32_e32 v35, vcc, 0, v35, vcc
	v_lshl_add_u64 v[4:5], v[4:5], 0, v[148:149]
	v_lshl_add_u64 v[2:3], v[2:3], 0, s[10:11]
	v_lshl_add_u64 v[152:153], v[4:5], 0, s[8:9]
	global_load_dwordx4 v[122:125], v[34:35], off offset:2560
	s_nop 0
	global_load_dwordx4 v[34:37], v[2:3], off offset:16
	global_load_dwordx4 v[126:129], v[38:39], off offset:32
	global_load_dwordx4 v[130:133], v[152:153], off offset:96
	global_load_dwordx4 v[134:137], v[152:153], off offset:64
	global_load_dwordx4 v[138:141], v[152:153], off offset:32
	v_add_co_u32_e32 v2, vcc, s20, v4
	s_lshl_b64 s[14:15], s[4:5], 12
	s_nop 0
	v_addc_co_u32_e32 v3, vcc, 0, v5, vcc
	global_load_dwordx4 v[2:5], v[2:3], off offset:512
	s_add_u32 s14, s13, s14
	s_addc_u32 s15, 0, s15
	v_lshl_add_u64 v[38:39], s[14:15], 0, v[142:143]
	v_lshlrev_b64 v[38:39], 14, v[38:39]
	s_mov_b32 s13, s5
	v_lshl_add_u64 v[38:39], s[84:85], 0, v[38:39]
	s_mov_b32 s0, 0
	v_lshl_add_u64 v[38:39], s[12:13], 2, v[38:39]
	v_mov_b32_e32 v151, v145
	v_lshl_add_u64 v[154:155], v[38:39], 0, v[150:151]
	s_mov_b32 s4, s0
	s_waitcnt vmcnt(20)
	v_lshlrev_b32_e32 v177, 16, v10
	s_waitcnt vmcnt(19)
	v_lshlrev_b32_e32 v168, 16, v14
	v_and_b32_e32 v169, 0xffff0000, v14
	v_lshlrev_b32_e32 v170, 16, v15
	v_lshlrev_b32_e32 v151, 16, v6
	v_and_b32_e32 v161, 0xffff0000, v6
	v_lshlrev_b32_e32 v162, 16, v7
	v_and_b32_e32 v163, 0xffff0000, v7
	v_lshlrev_b32_e32 v164, 16, v8
	v_and_b32_e32 v165, 0xffff0000, v8
	v_lshlrev_b32_e32 v166, 16, v9
	v_and_b32_e32 v167, 0xffff0000, v9
	v_and_b32_e32 v171, 0xffff0000, v15
	v_lshlrev_b32_e32 v172, 16, v16
	v_and_b32_e32 v173, 0xffff0000, v16
	v_lshlrev_b32_e32 v174, 16, v17
	v_and_b32_e32 v176, 0xffff0000, v17
	v_and_b32_e32 v178, 0xffff0000, v10
	v_lshlrev_b32_e32 v179, 16, v11
	v_and_b32_e32 v180, 0xffff0000, v11
	v_lshlrev_b32_e32 v181, 16, v12
	v_and_b32_e32 v182, 0xffff0000, v12
	v_lshlrev_b32_e32 v183, 16, v13
	v_and_b32_e32 v184, 0xffff0000, v13
	s_waitcnt vmcnt(13)
	v_lshlrev_b32_e32 v185, 16, v22
	v_and_b32_e32 v186, 0xffff0000, v22
	v_lshlrev_b32_e32 v187, 16, v23
	v_and_b32_e32 v188, 0xffff0000, v23
	v_lshlrev_b32_e32 v189, 16, v24
	v_and_b32_e32 v190, 0xffff0000, v24
	v_lshlrev_b32_e32 v191, 16, v25
	v_and_b32_e32 v192, 0xffff0000, v25
	v_lshlrev_b32_e32 v193, 16, v18
	v_and_b32_e32 v194, 0xffff0000, v18
	v_lshlrev_b32_e32 v195, 16, v19
	v_and_b32_e32 v196, 0xffff0000, v19
	v_lshlrev_b32_e32 v197, 16, v20
	v_and_b32_e32 v198, 0xffff0000, v20
	v_lshlrev_b32_e32 v199, 16, v21
	v_and_b32_e32 v200, 0xffff0000, v21
	s_waitcnt vmcnt(11)
	v_lshlrev_b32_e32 v201, 16, v30
	v_and_b32_e32 v202, 0xffff0000, v30
	v_lshlrev_b32_e32 v203, 16, v31
	v_and_b32_e32 v204, 0xffff0000, v31
	v_lshlrev_b32_e32 v205, 16, v32
	v_and_b32_e32 v206, 0xffff0000, v32
	v_lshlrev_b32_e32 v207, 16, v33
	v_and_b32_e32 v208, 0xffff0000, v33
	v_lshlrev_b32_e32 v209, 16, v26
	v_and_b32_e32 v210, 0xffff0000, v26
	v_lshlrev_b32_e32 v211, 16, v27
	v_and_b32_e32 v212, 0xffff0000, v27
	v_lshlrev_b32_e32 v213, 16, v28
	v_and_b32_e32 v214, 0xffff0000, v28
	v_lshlrev_b32_e32 v215, 16, v29
	v_and_b32_e32 v216, 0xffff0000, v29
	s_waitcnt vmcnt(5)
	v_lshlrev_b32_e32 v217, 16, v34
	v_and_b32_e32 v218, 0xffff0000, v34
	v_lshlrev_b32_e32 v219, 16, v35
	v_and_b32_e32 v220, 0xffff0000, v35
	v_lshlrev_b32_e32 v221, 16, v36
	v_and_b32_e32 v222, 0xffff0000, v36
	v_lshlrev_b32_e32 v223, 16, v37
	v_and_b32_e32 v224, 0xffff0000, v37
	s_cmp_lt_u32 s76, 4
	s_cbranch_scc1 .Lidx_noskew
	s_sleep 30
.Lidx_noskew:
	s_waitcnt vmcnt(0)
.LBB0_406:
	v_mfma_f32_32x32x16_bf16 v[50:65], v[74:77], v[2:5], 0
	s_add_i32 s1, s0, 1
	s_cmp_lt_i32 s1, s24
	s_cselect_b32 s12, s1, s0
	v_mad_u64_u32 v[234:235], s[12:13], s12, v159, v[152:153]
	s_mov_b32 s0, s1
	v_mfma_f32_32x32x16_bf16 v[34:49], v[90:93], v[2:5], 0
	v_mfma_f32_32x32x16_bf16 v[18:33], v[106:109], v[2:5], 0
	v_mfma_f32_32x32x16_bf16 v[2:17], v[122:125], v[2:5], 0
	v_mfma_f32_32x32x16_bf16 v[50:65], v[126:129], v[138:141], v[50:65]
	v_mfma_f32_32x32x16_bf16 v[34:49], v[78:81], v[138:141], v[34:49]
	v_mfma_f32_32x32x16_bf16 v[18:33], v[94:97], v[138:141], v[18:33]
	v_mfma_f32_32x32x16_bf16 v[2:17], v[110:113], v[138:141], v[2:17]
	global_load_dwordx4 v[138:141], v[234:235], off
	global_load_dwordx4 v[226:229], v[234:235], off offset:32
	global_load_dwordx4 v[230:233], v[234:235], off offset:64
	s_nop 0
	global_load_dwordx4 v[234:237], v[234:235], off offset:96
	v_mfma_f32_32x32x16_bf16 v[50:65], v[66:69], v[134:137], v[50:65]
	v_mfma_f32_32x32x16_bf16 v[34:49], v[82:85], v[134:137], v[34:49]
	v_mfma_f32_32x32x16_bf16 v[18:33], v[98:101], v[134:137], v[18:33]
	v_mfma_f32_32x32x16_bf16 v[2:17], v[114:117], v[134:137], v[2:17]
	v_lshl_add_u64 v[134:135], s[4:5], 2, v[154:155]
	v_add_co_u32_e32 v136, vcc, s21, v134
	s_add_i32 s4, s4, 32
	s_nop 0
	v_addc_co_u32_e32 v137, vcc, 0, v135, vcc
	v_add_co_u32_e32 v238, vcc, s22, v134
	v_mfma_f32_32x32x16_bf16 v[50:65], v[70:73], v[130:133], v[50:65]
	s_nop 0
	v_addc_co_u32_e32 v239, vcc, 0, v135, vcc
	v_add_co_u32_e32 v240, vcc, 0x18000, v134
	s_cmp_lg_u32 s24, s1
	s_nop 0
	v_addc_co_u32_e32 v241, vcc, 0, v135, vcc
	v_mfma_f32_32x32x16_bf16 v[34:49], v[86:89], v[130:133], v[34:49]
	s_nop 4
	v_med3_f32 v50, v50, 0, v160
	v_med3_f32 v51, v51, 0, v160
	v_fma_f32 v50, v151, v50, 0
	v_med3_f32 v52, v52, 0, v160
	v_fmac_f32_e32 v50, v161, v51
	v_med3_f32 v53, v53, 0, v160
	v_fmac_f32_e32 v50, v162, v52
	v_mfma_f32_32x32x16_bf16 v[18:33], v[102:105], v[130:133], v[18:33]
	v_med3_f32 v34, v34, 0, v160
	v_med3_f32 v35, v35, 0, v160
	v_fma_f32 v34, v177, v34, 0
	v_med3_f32 v36, v36, 0, v160
	v_fmac_f32_e32 v34, v178, v35
	v_med3_f32 v37, v37, 0, v160
	v_fmac_f32_e32 v34, v179, v36
	v_mfma_f32_32x32x16_bf16 v[2:17], v[118:121], v[130:133], v[2:17]
	s_nop 3
	v_med3_f32 v18, v18, 0, v160
	v_med3_f32 v19, v19, 0, v160
	v_fma_f32 v18, v193, v18, 0
	v_med3_f32 v20, v20, 0, v160
	v_fmac_f32_e32 v18, v194, v19
	v_med3_f32 v21, v21, 0, v160
	v_fmac_f32_e32 v18, v195, v20
	s_nop 0
	v_med3_f32 v2, v2, 0, v160
	v_med3_f32 v3, v3, 0, v160
	v_fma_f32 v2, v209, v2, 0
	v_med3_f32 v4, v4, 0, v160
	v_fmac_f32_e32 v2, v210, v3
	v_med3_f32 v5, v5, 0, v160
	v_fmac_f32_e32 v2, v211, v4
	v_med3_f32 v54, v54, 0, v160
	v_med3_f32 v38, v38, 0, v160
	v_med3_f32 v22, v22, 0, v160
	v_med3_f32 v6, v6, 0, v160
	v_fmac_f32_e32 v50, v163, v53
	v_fmac_f32_e32 v34, v180, v37
	v_fmac_f32_e32 v18, v196, v21
	v_fmac_f32_e32 v2, v212, v5
	v_med3_f32 v55, v55, 0, v160
	v_med3_f32 v39, v39, 0, v160
	v_med3_f32 v23, v23, 0, v160
	v_med3_f32 v7, v7, 0, v160
	v_fmac_f32_e32 v50, v164, v54
	v_fmac_f32_e32 v34, v181, v38
	v_fmac_f32_e32 v18, v197, v22
	v_fmac_f32_e32 v2, v213, v6
	v_med3_f32 v56, v56, 0, v160
	v_med3_f32 v40, v40, 0, v160
	v_med3_f32 v24, v24, 0, v160
	v_med3_f32 v8, v8, 0, v160
	v_fmac_f32_e32 v50, v165, v55
	v_fmac_f32_e32 v34, v182, v39
	v_fmac_f32_e32 v18, v198, v23
	v_fmac_f32_e32 v2, v214, v7
	v_med3_f32 v57, v57, 0, v160
	v_med3_f32 v41, v41, 0, v160
	v_med3_f32 v25, v25, 0, v160
	v_med3_f32 v9, v9, 0, v160
	v_fmac_f32_e32 v50, v166, v56
	v_fmac_f32_e32 v34, v183, v40
	v_fmac_f32_e32 v18, v199, v24
	v_fmac_f32_e32 v2, v215, v8
	v_med3_f32 v58, v58, 0, v160
	v_med3_f32 v42, v42, 0, v160
	v_med3_f32 v26, v26, 0, v160
	v_med3_f32 v10, v10, 0, v160
	v_fmac_f32_e32 v50, v167, v57
	v_fmac_f32_e32 v34, v184, v41
	v_fmac_f32_e32 v18, v200, v25
	v_fmac_f32_e32 v2, v216, v9
	v_med3_f32 v59, v59, 0, v160
	v_med3_f32 v43, v43, 0, v160
	v_med3_f32 v27, v27, 0, v160
	v_med3_f32 v11, v11, 0, v160
	v_fmac_f32_e32 v50, v168, v58
	v_fmac_f32_e32 v34, v185, v42
	v_fmac_f32_e32 v18, v201, v26
	v_fmac_f32_e32 v2, v217, v10
	v_med3_f32 v60, v60, 0, v160
	v_med3_f32 v44, v44, 0, v160
	v_med3_f32 v28, v28, 0, v160
	v_med3_f32 v12, v12, 0, v160
	v_fmac_f32_e32 v50, v169, v59
	v_fmac_f32_e32 v34, v186, v43
	v_fmac_f32_e32 v18, v202, v27
	v_fmac_f32_e32 v2, v218, v11
	v_med3_f32 v61, v61, 0, v160
	v_med3_f32 v45, v45, 0, v160
	v_med3_f32 v29, v29, 0, v160
	v_med3_f32 v13, v13, 0, v160
	v_fmac_f32_e32 v50, v170, v60
	v_fmac_f32_e32 v34, v187, v44
	v_fmac_f32_e32 v18, v203, v28
	v_fmac_f32_e32 v2, v219, v12
	v_med3_f32 v62, v62, 0, v160
	v_med3_f32 v46, v46, 0, v160
	v_med3_f32 v30, v30, 0, v160
	v_med3_f32 v14, v14, 0, v160
	v_fmac_f32_e32 v50, v171, v61
	v_fmac_f32_e32 v34, v188, v45
	v_fmac_f32_e32 v18, v204, v29
	v_fmac_f32_e32 v2, v220, v13
	v_med3_f32 v63, v63, 0, v160
	v_med3_f32 v47, v47, 0, v160
	v_med3_f32 v31, v31, 0, v160
	v_med3_f32 v15, v15, 0, v160
	v_fmac_f32_e32 v50, v172, v62
	v_fmac_f32_e32 v34, v189, v46
	v_fmac_f32_e32 v18, v205, v30
	v_fmac_f32_e32 v2, v221, v14
	v_med3_f32 v64, v64, 0, v160
	v_med3_f32 v48, v48, 0, v160
	v_med3_f32 v32, v32, 0, v160
	v_med3_f32 v16, v16, 0, v160
	v_fmac_f32_e32 v50, v173, v63
	v_fmac_f32_e32 v34, v190, v47
	v_fmac_f32_e32 v18, v206, v31
	v_fmac_f32_e32 v2, v222, v15
	v_med3_f32 v65, v65, 0, v160
	v_med3_f32 v49, v49, 0, v160
	v_med3_f32 v33, v33, 0, v160
	v_med3_f32 v17, v17, 0, v160
	v_fmac_f32_e32 v50, v174, v64
	v_fmac_f32_e32 v34, v191, v48
	v_fmac_f32_e32 v18, v207, v32
	v_fmac_f32_e32 v2, v223, v16
	v_fmac_f32_e32 v50, v176, v65
	v_fmac_f32_e32 v34, v192, v49
	v_fmac_f32_e32 v18, v208, v33
	v_fmac_f32_e32 v2, v224, v17
	v_mul_f32_e32 v3, 0x3d000000, v50
	v_mul_f32_e32 v4, 0x3d000000, v34
	v_mul_f32_e32 v5, 0x3d000000, v18
	v_mul_f32_e32 v2, 0x3d000000, v2
	global_store_dword v[134:135], v3, off
	global_store_dword v[136:137], v4, off
	global_store_dword v[238:239], v5, off
	global_store_dword v[240:241], v2, off
	s_waitcnt vmcnt(7)
	v_mov_b64_e32 v[2:3], v[138:139]
	v_mov_b64_e32 v[4:5], v[140:141]
	s_waitcnt vmcnt(6)
	v_mov_b64_e32 v[138:139], v[226:227]
	s_waitcnt vmcnt(5)
	v_mov_b64_e32 v[134:135], v[230:231]
	s_waitcnt vmcnt(4)
	v_mov_b64_e32 v[130:131], v[234:235]
	v_mov_b64_e32 v[140:141], v[228:229]
	v_mov_b64_e32 v[136:137], v[232:233]
	v_mov_b64_e32 v[132:133], v[236:237]
	s_cbranch_scc1 .LBB0_406
